# phase-5 B-fragment LDS addresses precomputed as well, wave-uniform ballot in phase 3 replaced by one s_not_b64
# baseline (speedup 1.0000x reference)
.LBB2_32:
	s_xor_b64 s[30:31], s[4:5], -1
	s_lshl_b32 s4, s63, 8
	s_ashr_i32 s5, s4, 31
	s_lshl_b64 s[4:5], s[4:5], 11
	s_add_u32 s4, s14, s4
	s_addc_u32 s5, s15, s5
	s_add_u32 s24, s4, 0x400000
	s_addc_u32 s25, s5, 0
	s_and_b64 s[4:5], s[28:29], exec
	s_cselect_b32 s66, s25, s19
	s_cselect_b32 s67, s24, s18
	s_lshl_b32 s4, s62, 8
	s_ashr_i32 s5, s4, 31
	s_lshl_b64 s[4:5], s[4:5], 11
	s_add_u32 s26, s12, s4
	s_addc_u32 s27, s13, s5
	s_and_b64 s[4:5], s[28:29], exec
	s_cselect_b32 s68, s27, s1
	s_cselect_b32 s69, s26, s0
	s_add_u32 s70, s18, 0x40080
	s_addc_u32 s71, s19, 0
	s_add_u32 s72, s0, 0x100
	v_mov_b64_e32 v[0:1], 0
	s_addc_u32 s73, s1, 0
	s_mov_b32 s74, -2
	v_mov_b64_e32 v[2:3], 0
	v_mov_b64_e32 v[4:5], 0
	v_mov_b64_e32 v[6:7], 0
	v_mov_b64_e32 v[8:9], 0
	v_mov_b64_e32 v[10:11], 0
	v_mov_b64_e32 v[12:13], 0
	v_mov_b64_e32 v[14:15], 0
	v_mov_b64_e32 v[16:17], 0
	v_mov_b64_e32 v[18:19], 0
	v_mov_b64_e32 v[20:21], 0
	v_mov_b64_e32 v[22:23], 0
	v_mov_b64_e32 v[24:25], 0
	v_mov_b64_e32 v[26:27], 0
	v_mov_b64_e32 v[28:29], 0
	v_mov_b64_e32 v[30:31], 0
	v_mov_b64_e32 v[32:33], 0
	v_mov_b64_e32 v[34:35], 0
	v_mov_b64_e32 v[36:37], 0
	v_mov_b64_e32 v[38:39], 0
	v_mov_b64_e32 v[40:41], 0
	v_mov_b64_e32 v[42:43], 0
	v_mov_b64_e32 v[44:45], 0
	v_mov_b64_e32 v[46:47], 0
	v_mov_b64_e32 v[48:49], 0
	v_mov_b64_e32 v[50:51], 0
	v_mov_b64_e32 v[52:53], 0
	v_mov_b64_e32 v[54:55], 0
	v_mov_b64_e32 v[56:57], 0
	v_mov_b64_e32 v[58:59], 0
	v_mov_b64_e32 v[60:61], 0
	v_mov_b64_e32 v[62:63], 0
	v_mov_b64_e32 v[64:65], 0
	v_mov_b64_e32 v[66:67], 0
	v_mov_b64_e32 v[68:69], 0
	v_mov_b64_e32 v[70:71], 0
	v_mov_b64_e32 v[72:73], 0
	v_mov_b64_e32 v[74:75], 0
	v_mov_b64_e32 v[76:77], 0
	v_mov_b64_e32 v[78:79], 0
	v_mov_b64_e32 v[80:81], 0
	v_mov_b64_e32 v[82:83], 0
	v_mov_b64_e32 v[84:85], 0
	v_mov_b64_e32 v[86:87], 0
	v_mov_b64_e32 v[88:89], 0
	v_mov_b64_e32 v[90:91], 0
	v_mov_b64_e32 v[92:93], 0
	v_mov_b64_e32 v[94:95], 0
	v_mov_b64_e32 v[96:97], 0
	v_mov_b64_e32 v[98:99], 0
	v_mov_b64_e32 v[100:101], 0
	v_mov_b64_e32 v[102:103], 0
	v_mov_b64_e32 v[104:105], 0
	v_mov_b64_e32 v[106:107], 0
	v_mov_b64_e32 v[108:109], 0
	v_mov_b64_e32 v[110:111], 0
	v_mov_b64_e32 v[112:113], 0
	v_mov_b64_e32 v[114:115], 0
	v_mov_b64_e32 v[116:117], 0
	v_mov_b64_e32 v[118:119], 0
	v_mov_b64_e32 v[120:121], 0
	v_mov_b64_e32 v[122:123], 0
	v_mov_b64_e32 v[124:125], 0
	v_mov_b64_e32 v[126:127], 0
	s_waitcnt lgkmcnt(0)
	v_add_u32_e32 v212, 0x1c000, v199
	v_add_u32_e32 v213, 0x1c000, v200
	v_add_u32_e32 v210, 0x18000, v199
	v_add_u32_e32 v211, 0x18000, v200
	s_branch .LBB2_34

.LBB2_36:
	s_add_u32 s4, s70, 0xfffc0080
	s_addc_u32 s5, s71, -1
	s_barrier
	s_waitcnt lgkmcnt(0)
	s_setprio 1
	v_mfma_i32_16x16x64_i8 v[116:119], v[128:131], v[184:187], v[116:119]
	s_and_b64 s[0:1], s[0:1], exec
	s_cselect_b32 s17, s5, s66
	s_cselect_b32 s4, s4, s67
	v_mfma_i32_16x16x64_i8 v[112:115], v[132:135], v[184:187], v[112:115]
	v_mfma_i32_16x16x64_i8 v[100:103], v[128:131], v[172:175], v[100:103]
	v_mfma_i32_16x16x64_i8 v[92:95], v[132:135], v[172:175], v[92:95]
	v_mfma_i32_16x16x64_i8 v[84:87], v[128:131], v[168:171], v[84:87]
	v_mfma_i32_16x16x64_i8 v[76:79], v[132:135], v[168:171], v[76:79]
	v_mfma_i32_16x16x64_i8 v[68:71], v[128:131], v[160:163], v[68:71]
	v_mfma_i32_16x16x64_i8 v[64:67], v[132:135], v[160:163], v[64:67]
	v_mfma_i32_16x16x64_i8 v[116:119], v[140:143], v[188:191], v[116:119]
	v_mfma_i32_16x16x64_i8 v[112:115], v[136:139], v[188:191], v[112:115]
	v_mfma_i32_16x16x64_i8 v[100:103], v[140:143], v[176:179], v[100:103]
	v_mfma_i32_16x16x64_i8 v[92:95], v[136:139], v[176:179], v[92:95]
	v_mfma_i32_16x16x64_i8 v[84:87], v[140:143], v[180:183], v[84:87]
	v_mfma_i32_16x16x64_i8 v[76:79], v[136:139], v[180:183], v[76:79]
	v_mfma_i32_16x16x64_i8 v[68:71], v[140:143], v[164:167], v[68:71]
	v_mfma_i32_16x16x64_i8 v[64:67], v[136:139], v[164:167], v[64:67]
	s_setprio 0
	s_barrier
	ds_read_b128 v[184:187], v205 offset:16384
	ds_read_b128 v[172:175], v205 offset:18432
	ds_read_b128 v[188:191], v206 offset:16384
	ds_read_b128 v[176:179], v206 offset:18432
	ds_read_b128 v[168:171], v205 offset:20480
	ds_read_b128 v[160:163], v205 offset:22528
	ds_read_b128 v[180:183], v206 offset:20480
	ds_read_b128 v[164:167], v206 offset:22528
	s_not_b64 s[0:1], s[36:37]
	s_andn2_b64 vcc, exec, s[36:37]
	s_cbranch_vccnz .LBB2_38
	s_and_b32 s5, s17, 0xffff
	s_mov_b32 m0, s38
	s_nop 0
	buffer_load_dwordx4 v193, s[4:7], 0 offen lds
	s_mov_b32 m0, s41
	s_nop 0
	buffer_load_dwordx4 v197, s[4:7], 0 offen lds

.LBB2_42:
	s_barrier
	s_setprio 1
	v_mfma_i32_16x16x64_i8 v[48:51], v[128:131], v[184:187], v[48:51]
	v_mfma_i32_16x16x64_i8 v[40:43], v[132:135], v[184:187], v[40:43]
	v_mfma_i32_16x16x64_i8 v[32:35], v[128:131], v[172:175], v[32:35]
	v_mfma_i32_16x16x64_i8 v[24:27], v[132:135], v[172:175], v[24:27]
	v_mfma_i32_16x16x64_i8 v[16:19], v[128:131], v[168:171], v[16:19]
	v_mfma_i32_16x16x64_i8 v[8:11], v[132:135], v[168:171], v[8:11]
	v_mfma_i32_16x16x64_i8 v[4:7], v[128:131], v[160:163], v[4:7]
	v_mfma_i32_16x16x64_i8 v[0:3], v[132:135], v[160:163], v[0:3]
	v_mfma_i32_16x16x64_i8 v[48:51], v[140:143], v[188:191], v[48:51]
	v_mfma_i32_16x16x64_i8 v[40:43], v[136:139], v[188:191], v[40:43]
	v_mfma_i32_16x16x64_i8 v[32:35], v[140:143], v[176:179], v[32:35]
	v_mfma_i32_16x16x64_i8 v[24:27], v[136:139], v[176:179], v[24:27]
	v_mfma_i32_16x16x64_i8 v[16:19], v[140:143], v[180:183], v[16:19]
	v_mfma_i32_16x16x64_i8 v[8:11], v[136:139], v[180:183], v[8:11]
	v_mfma_i32_16x16x64_i8 v[4:7], v[140:143], v[164:167], v[4:7]
	v_mfma_i32_16x16x64_i8 v[0:3], v[136:139], v[164:167], v[0:3]
	s_setprio 0
	s_barrier
	ds_read_b128 v[128:131], v210
	ds_read_b128 v[132:135], v210 offset:2048
	ds_read_b128 v[140:143], v211
	ds_read_b128 v[136:139], v211 offset:2048
	ds_read_b128 v[184:187], v205 offset:32768
	ds_read_b128 v[172:175], v205 offset:34816
	ds_read_b128 v[188:191], v206 offset:32768
	ds_read_b128 v[176:179], v206 offset:34816
	ds_read_b128 v[168:171], v205 offset:36864
	ds_read_b128 v[160:163], v205 offset:38912
	ds_read_b128 v[180:183], v206 offset:36864
	ds_read_b128 v[164:167], v206 offset:38912
	s_and_b64 vcc, exec, s[0:1]
	s_cbranch_vccnz .LBB2_44
	s_add_u32 s76, s4, 0x40000
	s_addc_u32 s5, s17, 0
	s_and_b32 s77, s5, 0xffff
	s_mov_b32 s78, s6
	s_mov_b32 s79, s7
	s_mov_b32 m0, s44
	s_nop 0
	buffer_load_dwordx4 v193, s[76:79], 0 offen lds
	s_mov_b32 m0, s45
	s_nop 0
	buffer_load_dwordx4 v197, s[76:79], 0 offen lds

.Lp2_sum_skip:
	s_barrier
	buffer_load_dwordx4 v194, s[12:15], 0 offen lds
	s_mov_b32 m0, s41
	v_lshrrev_b32_e32 v2, 4, v0
	buffer_load_dwordx4 v196, s[12:15], 0 offen lds
	s_add_u32 s12, s16, 0x80
	s_addc_u32 s0, s9, 0
	s_add_i32 s42, s31, 0x8000
	s_and_b32 s13, s0, 0xffff
	s_mov_b32 m0, s42
	s_add_i32 s43, s31, 0xa000
	buffer_load_dwordx4 v1, s[12:15], 0 offen lds
	s_mov_b32 m0, s43
	v_and_b32_e32 v197, 15, v0
	buffer_load_dwordx4 v195, s[12:15], 0 offen lds
	s_add_u32 s12, s8, 0x10080
	s_addc_u32 s0, s25, 0
	s_add_i32 s44, s31, 0x1c000
	s_and_b32 s13, s0, 0xffff
	s_mov_b32 m0, s44
	s_add_i32 s45, s31, 0x1e000
	buffer_load_dwordx4 v194, s[12:15], 0 offen lds
	s_mov_b32 m0, s45
	s_and_b32 s0, s2, 1
	buffer_load_dwordx4 v196, s[12:15], 0 offen lds
	s_lshl_b32 s0, s0, 23
	s_lshl_b32 s1, s26, 21
	v_bfe_u32 v3, v0, 1, 3
	s_or_b32 s0, s0, s1
	v_bitop3_b32 v2, v2, v3, 3 bitop3:0x6c
	v_lshlrev_b32_e32 v3, 7, v197
	s_add_i32 s46, s31, 0xc000
	s_add_i32 s47, s31, 0xe000
	s_or_b32 s0, s27, s0
	v_lshlrev_b32_e32 v2, 4, v2
	v_lshl_or_b32 v4, s28, 13, v3
	v_lshl_or_b32 v3, s39, 12, v3
	s_waitcnt vmcnt(6)
	s_add_u32 s48, s20, s0
	v_or_b32_e32 v5, v4, v2
	v_bitop3_b32 v4, v4, 64, v2 bitop3:0x36
	v_or_b32_e32 v198, v3, v2
	v_bitop3_b32 v199, v3, 64, v2 bitop3:0x36
	s_addc_u32 s49, s21, 0
	v_mov_b32_e32 v66, 0
	s_add_i32 s0, 0, 0x10000
	s_add_i32 s1, 0, 0x14000
	s_mov_b32 s50, -2
	s_mov_b64 s[10:11], 0
	v_add_u32_e32 v200, 0, v5
	v_add_u32_e32 v201, 0, v4
	v_mov_b32_e32 v67, v66
	v_mov_b32_e32 v68, v66
	v_mov_b32_e32 v69, v66
	v_mov_b32_e32 v70, v66
	v_mov_b32_e32 v71, v66
	v_mov_b32_e32 v72, v66
	v_mov_b32_e32 v73, v66
	v_mov_b32_e32 v82, v66
	v_mov_b32_e32 v83, v66
	v_mov_b32_e32 v84, v66
	v_mov_b32_e32 v85, v66
	v_mov_b32_e32 v86, v66
	v_mov_b32_e32 v87, v66
	v_mov_b32_e32 v88, v66
	v_mov_b32_e32 v89, v66
	v_mov_b32_e32 v98, v66
	v_mov_b32_e32 v99, v66
	v_mov_b32_e32 v100, v66
	v_mov_b32_e32 v101, v66
	v_mov_b32_e32 v102, v66
	v_mov_b32_e32 v103, v66
	v_mov_b32_e32 v104, v66
	v_mov_b32_e32 v105, v66
	v_mov_b32_e32 v114, v66
	v_mov_b32_e32 v115, v66
	v_mov_b32_e32 v116, v66
	v_mov_b32_e32 v117, v66
	v_mov_b32_e32 v118, v66
	v_mov_b32_e32 v119, v66
	v_mov_b32_e32 v120, v66
	v_mov_b32_e32 v121, v66
	v_mov_b32_e32 v74, v66
	v_mov_b32_e32 v75, v66
	v_mov_b32_e32 v76, v66
	v_mov_b32_e32 v77, v66
	v_mov_b32_e32 v78, v66
	v_mov_b32_e32 v79, v66
	v_mov_b32_e32 v80, v66
	v_mov_b32_e32 v81, v66
	v_mov_b32_e32 v90, v66
	v_mov_b32_e32 v91, v66
	v_mov_b32_e32 v92, v66
	v_mov_b32_e32 v93, v66
	v_mov_b32_e32 v94, v66
	v_mov_b32_e32 v95, v66
	v_mov_b32_e32 v96, v66
	v_mov_b32_e32 v97, v66
	v_mov_b32_e32 v106, v66
	v_mov_b32_e32 v107, v66
	v_mov_b32_e32 v108, v66
	v_mov_b32_e32 v109, v66
	v_mov_b32_e32 v110, v66
	v_mov_b32_e32 v111, v66
	v_mov_b32_e32 v112, v66
	v_mov_b32_e32 v113, v66
	v_mov_b32_e32 v122, v66
	v_mov_b32_e32 v123, v66
	v_mov_b32_e32 v124, v66
	v_mov_b32_e32 v125, v66
	v_mov_b32_e32 v126, v66
	v_mov_b32_e32 v127, v66
	v_mov_b32_e32 v128, v66
	v_mov_b32_e32 v129, v66
	v_mov_b32_e32 v130, v66
	v_mov_b32_e32 v131, v66
	v_mov_b32_e32 v132, v66
	v_mov_b32_e32 v133, v66
	v_mov_b32_e32 v134, v66
	v_mov_b32_e32 v135, v66
	v_mov_b32_e32 v136, v66
	v_mov_b32_e32 v137, v66
	v_mov_b32_e32 v146, v66
	v_mov_b32_e32 v147, v66
	v_mov_b32_e32 v148, v66
	v_mov_b32_e32 v149, v66
	v_mov_b32_e32 v150, v66
	v_mov_b32_e32 v151, v66
	v_mov_b32_e32 v152, v66
	v_mov_b32_e32 v153, v66
	v_mov_b32_e32 v162, v66
	v_mov_b32_e32 v163, v66
	v_mov_b32_e32 v164, v66
	v_mov_b32_e32 v165, v66
	v_mov_b32_e32 v166, v66
	v_mov_b32_e32 v167, v66
	v_mov_b32_e32 v168, v66
	v_mov_b32_e32 v169, v66
	v_mov_b32_e32 v178, v66
	v_mov_b32_e32 v179, v66
	v_mov_b32_e32 v180, v66
	v_mov_b32_e32 v181, v66
	v_mov_b32_e32 v182, v66
	v_mov_b32_e32 v183, v66
	v_mov_b32_e32 v184, v66
	v_mov_b32_e32 v185, v66
	v_mov_b32_e32 v138, v66
	v_mov_b32_e32 v139, v66
	v_mov_b32_e32 v140, v66
	v_mov_b32_e32 v141, v66
	v_mov_b32_e32 v142, v66
	v_mov_b32_e32 v143, v66
	v_mov_b32_e32 v144, v66
	v_mov_b32_e32 v145, v66
	v_mov_b32_e32 v154, v66
	v_mov_b32_e32 v155, v66
	v_mov_b32_e32 v156, v66
	v_mov_b32_e32 v157, v66
	v_mov_b32_e32 v158, v66
	v_mov_b32_e32 v159, v66
	v_mov_b32_e32 v160, v66
	v_mov_b32_e32 v161, v66
	v_mov_b32_e32 v170, v66
	v_mov_b32_e32 v171, v66
	v_mov_b32_e32 v172, v66
	v_mov_b32_e32 v173, v66
	v_mov_b32_e32 v174, v66
	v_mov_b32_e32 v175, v66
	v_mov_b32_e32 v176, v66
	v_mov_b32_e32 v177, v66
	v_mov_b32_e32 v186, v66
	v_mov_b32_e32 v187, v66
	v_mov_b32_e32 v188, v66
	v_mov_b32_e32 v189, v66
	v_mov_b32_e32 v190, v66
	v_mov_b32_e32 v191, v66
	v_mov_b32_e32 v192, v66
	v_mov_b32_e32 v193, v66
	v_bfe_u32 v202, v0, 4, 2
	v_add_u32_e32 v203, s0, v198
	v_add_u32_e32 v204, s0, v199
	v_add_u32_e32 v205, s1, v198
	v_add_u32_e32 v206, s1, v199
	s_barrier
	s_cmpk_eq_i32 s10, 0x700
	s_cselect_b64 s[18:19], -1, 0
	s_cmpk_lg_i32 s10, 0x700
	s_cselect_b64 s[26:27], -1, 0
	s_add_u32 s54, s48, s10
	s_addc_u32 s55, s49, s11
	s_add_u32 s51, s8, s10
	s_addc_u32 s52, s25, s11
	s_add_u32 s20, s51, 0x100
	s_addc_u32 s53, s52, 0
	s_add_u32 s12, s54, 0x100080
	s_addc_u32 s0, s55, 0
	s_and_b32 s13, s0, 0xffff
	v_add_u32_e32 v210, 0x1c000, v198
	v_add_u32_e32 v211, 0x1c000, v199
	v_add_u32_e32 v212, 0x18000, v198
	v_add_u32_e32 v213, 0x18000, v199
	s_branch .LBB3_4

.LBB3_6:
	s_barrier
	s_waitcnt lgkmcnt(0)
	s_setprio 1
	v_mfma_f32_16x16x128_f8f6f4 v[182:185], v[26:33], v[58:65], v[182:185]
	s_add_u32 s12, s54, 0x100
	s_addc_u32 s21, s55, 0
	v_mfma_f32_16x16x128_f8f6f4 v[178:181], v[18:25], v[58:65], v[178:181]
	v_mfma_f32_16x16x128_f8f6f4 v[166:169], v[26:33], v[50:57], v[166:169]
	v_mfma_f32_16x16x128_f8f6f4 v[162:165], v[18:25], v[50:57], v[162:165]
	v_mfma_f32_16x16x128_f8f6f4 v[150:153], v[26:33], v[42:49], v[150:153]
	v_mfma_f32_16x16x128_f8f6f4 v[146:149], v[18:25], v[42:49], v[146:149]
	v_mfma_f32_16x16x128_f8f6f4 v[134:137], v[26:33], v[34:41], v[134:137]
	v_mfma_f32_16x16x128_f8f6f4 v[130:133], v[18:25], v[34:41], v[130:133]
	s_setprio 0
	s_barrier
	ds_read_b128 v[58:61], v200 offset:16384
	ds_read_b128 v[50:53], v200 offset:18432
	ds_read_b128 v[62:65], v201 offset:16384
	ds_read_b128 v[54:57], v201 offset:18432
	ds_read_b128 v[42:45], v200 offset:20480
	ds_read_b128 v[34:37], v200 offset:22528
	ds_read_b128 v[46:49], v201 offset:20480
	ds_read_b128 v[38:41], v201 offset:22528
	s_not_b64 s[0:1], s[26:27]
	s_andn2_b64 vcc, exec, s[26:27]
	s_cbranch_vccnz .LBB3_8
	s_and_b32 s13, s21, 0xffff
	s_mov_b32 m0, s31
	s_nop 0
	buffer_load_dwordx4 v1, s[12:15], 0 offen lds
	s_mov_b32 m0, s35
	s_nop 0
	buffer_load_dwordx4 v195, s[12:15], 0 offen lds

.LBB3_12:
	s_barrier
	s_setprio 1
	v_mfma_f32_16x16x128_f8f6f4 v[118:121], v[26:33], v[58:65], v[118:121]
	v_mfma_f32_16x16x128_f8f6f4 v[114:117], v[18:25], v[58:65], v[114:117]
	v_mfma_f32_16x16x128_f8f6f4 v[102:105], v[26:33], v[50:57], v[102:105]
	v_mfma_f32_16x16x128_f8f6f4 v[98:101], v[18:25], v[50:57], v[98:101]
	v_mfma_f32_16x16x128_f8f6f4 v[86:89], v[26:33], v[42:49], v[86:89]
	v_mfma_f32_16x16x128_f8f6f4 v[82:85], v[18:25], v[42:49], v[82:85]
	v_mfma_f32_16x16x128_f8f6f4 v[70:73], v[26:33], v[34:41], v[70:73]
	v_mfma_f32_16x16x128_f8f6f4 v[66:69], v[18:25], v[34:41], v[66:69]
	s_setprio 0
	s_barrier
	ds_read_b128 v[10:13], v212
	ds_read_b128 v[2:5], v212 offset:2048
	ds_read_b128 v[14:17], v213
	ds_read_b128 v[6:9], v213 offset:2048
	ds_read_b128 v[58:61], v200 offset:32768
	ds_read_b128 v[50:53], v200 offset:34816
	ds_read_b128 v[62:65], v201 offset:32768
	ds_read_b128 v[54:57], v201 offset:34816
	ds_read_b128 v[42:45], v200 offset:36864
	ds_read_b128 v[34:37], v200 offset:38912
	ds_read_b128 v[46:49], v201 offset:36864
	ds_read_b128 v[38:41], v201 offset:38912
	s_waitcnt vmcnt(8)
	s_and_b64 vcc, exec, s[0:1]
	s_cbranch_vccnz .LBB3_14
	s_add_u32 s56, s54, 0x100100
	s_addc_u32 s13, s55, 0
	s_and_b32 s57, s13, 0xffff
	s_mov_b32 s58, s14
	s_mov_b32 s59, s15
	s_mov_b32 m0, s37
	s_nop 0
	buffer_load_dwordx4 v1, s[56:59], 0 offen lds
	s_mov_b32 m0, s38
	s_nop 0
	buffer_load_dwordx4 v195, s[56:59], 0 offen lds

	.amdhsa_kernel _ZN2rb6k_gemmILi1ENS_7SchedP2ENS_7EpiSlabEEEvT0_T1_
		.amdhsa_group_segment_fixed_size 0
		.amdhsa_private_segment_fixed_size 0
		.amdhsa_kernarg_size 40
		.amdhsa_user_sgpr_count 2
		.amdhsa_user_sgpr_dispatch_ptr 0
		.amdhsa_user_sgpr_queue_ptr 0
		.amdhsa_user_sgpr_kernarg_segment_ptr 1
		.amdhsa_user_sgpr_dispatch_id 0
		.amdhsa_user_sgpr_kernarg_preload_length 0
		.amdhsa_user_sgpr_kernarg_preload_offset 0
		.amdhsa_user_sgpr_private_segment_size 0
		.amdhsa_uses_dynamic_stack 0
		.amdhsa_enable_private_segment 0
		.amdhsa_system_sgpr_workgroup_id_x 1
		.amdhsa_system_sgpr_workgroup_id_y 0
		.amdhsa_system_sgpr_workgroup_id_z 0
		.amdhsa_system_sgpr_workgroup_info 0
		.amdhsa_system_vgpr_workitem_id 0
		.amdhsa_next_free_vgpr 214
		.amdhsa_next_free_sgpr 67
		.amdhsa_accum_offset 216
		.amdhsa_reserve_vcc 1
		.amdhsa_float_round_mode_32 0
		.amdhsa_float_round_mode_16_64 0
		.amdhsa_float_denorm_mode_32 3
		.amdhsa_float_denorm_mode_16_64 3
		.amdhsa_dx10_clamp 1
		.amdhsa_ieee_mode 1
		.amdhsa_fp16_overflow 0
		.amdhsa_tg_split 0
		.amdhsa_exception_fp_ieee_invalid_op 0
		.amdhsa_exception_fp_denorm_src 0
		.amdhsa_exception_fp_ieee_div_zero 0
		.amdhsa_exception_fp_ieee_overflow 0
		.amdhsa_exception_fp_ieee_underflow 0
		.amdhsa_exception_fp_ieee_inexact 0
		.amdhsa_exception_int_div_zero 0
	.end_amdhsa_kernel

.LBB4_12:
	s_and_b32 s33, s0, 3
	s_add_u32 s12, s8, 0x80
	s_addc_u32 s0, s3, 0
	s_add_i32 s36, s7, 0x18000
	s_and_b32 s13, s0, 0xffff
	s_mov_b32 m0, s36
	s_add_i32 s37, s7, 0x1a000
	s_waitcnt vmcnt(4)
	s_barrier
	buffer_load_dwordx4 v193, s[12:15], 0 offen lds
	s_mov_b32 m0, s37
	v_lshrrev_b32_e32 v1, 4, v0
	buffer_load_dwordx4 v195, s[12:15], 0 offen lds
	s_add_u32 s12, s16, 0x80
	s_addc_u32 s0, s9, 0
	s_add_i32 s38, s7, 0x8000
	s_and_b32 s13, s0, 0xffff
	s_mov_b32 m0, s38
	s_add_i32 s39, s7, 0xa000
	buffer_load_dwordx4 v192, s[12:15], 0 offen lds
	s_mov_b32 m0, s39
	v_and_b32_e32 v196, 15, v0
	buffer_load_dwordx4 v194, s[12:15], 0 offen lds
	s_add_u32 s12, s8, 0x4080
	s_addc_u32 s0, s3, 0
	s_add_i32 s40, s7, 0x1c000
	s_and_b32 s13, s0, 0xffff
	s_mov_b32 m0, s40
	s_add_i32 s41, s7, 0x1e000
	buffer_load_dwordx4 v193, s[12:15], 0 offen lds
	s_mov_b32 m0, s41
	v_bfe_u32 v197, v0, 4, 2
	buffer_load_dwordx4 v195, s[12:15], 0 offen lds
	v_bfe_u32 v0, v0, 1, 3
	v_bitop3_b32 v0, v1, v0, 3 bitop3:0x6c
	v_lshlrev_b32_e32 v1, 7, v196
	v_lshlrev_b32_e32 v0, 4, v0
	v_lshl_or_b32 v2, s27, 13, v1
	v_lshl_or_b32 v1, s33, 12, v1
	s_waitcnt vmcnt(6)
	v_or_b32_e32 v3, v2, v0
	v_or_b32_e32 v198, v1, v0
	v_bitop3_b32 v2, v2, 64, v0 bitop3:0x36
	v_bitop3_b32 v199, v1, 64, v0 bitop3:0x36
	v_mov_b32_e32 v64, 0
	s_add_i32 s0, 0, 0x10000
	s_add_i32 s1, 0, 0x14000
	s_add_i32 s42, s7, 0xc000
	s_add_i32 s43, s7, 0xe000
	s_mov_b32 s44, -2
	s_mov_b64 s[10:11], 0
	v_add_u32_e32 v200, 0, v3
	v_add_u32_e32 v201, 0, v2
	s_add_i32 s45, 0, 0x18000
	v_mov_b32_e32 v65, v64
	v_mov_b32_e32 v66, v64
	v_mov_b32_e32 v67, v64
	v_mov_b32_e32 v68, v64
	v_mov_b32_e32 v69, v64
	v_mov_b32_e32 v70, v64
	v_mov_b32_e32 v71, v64
	v_mov_b32_e32 v80, v64
	v_mov_b32_e32 v81, v64
	v_mov_b32_e32 v82, v64
	v_mov_b32_e32 v83, v64
	v_mov_b32_e32 v84, v64
	v_mov_b32_e32 v85, v64
	v_mov_b32_e32 v86, v64
	v_mov_b32_e32 v87, v64
	v_mov_b32_e32 v96, v64
	v_mov_b32_e32 v97, v64
	v_mov_b32_e32 v98, v64
	v_mov_b32_e32 v99, v64
	v_mov_b32_e32 v100, v64
	v_mov_b32_e32 v101, v64
	v_mov_b32_e32 v102, v64
	v_mov_b32_e32 v103, v64
	v_mov_b32_e32 v112, v64
	v_mov_b32_e32 v113, v64
	v_mov_b32_e32 v114, v64
	v_mov_b32_e32 v115, v64
	v_mov_b32_e32 v116, v64
	v_mov_b32_e32 v117, v64
	v_mov_b32_e32 v118, v64
	v_mov_b32_e32 v119, v64
	v_mov_b32_e32 v72, v64
	v_mov_b32_e32 v73, v64
	v_mov_b32_e32 v74, v64
	v_mov_b32_e32 v75, v64
	v_mov_b32_e32 v76, v64
	v_mov_b32_e32 v77, v64
	v_mov_b32_e32 v78, v64
	v_mov_b32_e32 v79, v64
	v_mov_b32_e32 v88, v64
	v_mov_b32_e32 v89, v64
	v_mov_b32_e32 v90, v64
	v_mov_b32_e32 v91, v64
	v_mov_b32_e32 v92, v64
	v_mov_b32_e32 v93, v64
	v_mov_b32_e32 v94, v64
	v_mov_b32_e32 v95, v64
	v_mov_b32_e32 v104, v64
	v_mov_b32_e32 v105, v64
	v_mov_b32_e32 v106, v64
	v_mov_b32_e32 v107, v64
	v_mov_b32_e32 v108, v64
	v_mov_b32_e32 v109, v64
	v_mov_b32_e32 v110, v64
	v_mov_b32_e32 v111, v64
	v_mov_b32_e32 v120, v64
	v_mov_b32_e32 v121, v64
	v_mov_b32_e32 v122, v64
	v_mov_b32_e32 v123, v64
	v_mov_b32_e32 v124, v64
	v_mov_b32_e32 v125, v64
	v_mov_b32_e32 v126, v64
	v_mov_b32_e32 v127, v64
	v_mov_b32_e32 v128, v64
	v_mov_b32_e32 v129, v64
	v_mov_b32_e32 v130, v64
	v_mov_b32_e32 v131, v64
	v_mov_b32_e32 v132, v64
	v_mov_b32_e32 v133, v64
	v_mov_b32_e32 v134, v64
	v_mov_b32_e32 v135, v64
	v_mov_b32_e32 v144, v64
	v_mov_b32_e32 v145, v64
	v_mov_b32_e32 v146, v64
	v_mov_b32_e32 v147, v64
	v_mov_b32_e32 v148, v64
	v_mov_b32_e32 v149, v64
	v_mov_b32_e32 v150, v64
	v_mov_b32_e32 v151, v64
	v_mov_b32_e32 v160, v64
	v_mov_b32_e32 v161, v64
	v_mov_b32_e32 v162, v64
	v_mov_b32_e32 v163, v64
	v_mov_b32_e32 v164, v64
	v_mov_b32_e32 v165, v64
	v_mov_b32_e32 v166, v64
	v_mov_b32_e32 v167, v64
	v_mov_b32_e32 v176, v64
	v_mov_b32_e32 v177, v64
	v_mov_b32_e32 v178, v64
	v_mov_b32_e32 v179, v64
	v_mov_b32_e32 v180, v64
	v_mov_b32_e32 v181, v64
	v_mov_b32_e32 v182, v64
	v_mov_b32_e32 v183, v64
	v_mov_b32_e32 v136, v64
	v_mov_b32_e32 v137, v64
	v_mov_b32_e32 v138, v64
	v_mov_b32_e32 v139, v64
	v_mov_b32_e32 v140, v64
	v_mov_b32_e32 v141, v64
	v_mov_b32_e32 v142, v64
	v_mov_b32_e32 v143, v64
	v_mov_b32_e32 v152, v64
	v_mov_b32_e32 v153, v64
	v_mov_b32_e32 v154, v64
	v_mov_b32_e32 v155, v64
	v_mov_b32_e32 v156, v64
	v_mov_b32_e32 v157, v64
	v_mov_b32_e32 v158, v64
	v_mov_b32_e32 v159, v64
	v_mov_b32_e32 v168, v64
	v_mov_b32_e32 v169, v64
	v_mov_b32_e32 v170, v64
	v_mov_b32_e32 v171, v64
	v_mov_b32_e32 v172, v64
	v_mov_b32_e32 v173, v64
	v_mov_b32_e32 v174, v64
	v_mov_b32_e32 v175, v64
	v_mov_b32_e32 v184, v64
	v_mov_b32_e32 v185, v64
	v_mov_b32_e32 v186, v64
	v_mov_b32_e32 v187, v64
	v_mov_b32_e32 v188, v64
	v_mov_b32_e32 v189, v64
	v_mov_b32_e32 v190, v64
	v_mov_b32_e32 v191, v64
	v_add_u32_e32 v202, s0, v198
	v_add_u32_e32 v203, s0, v199
	v_add_u32_e32 v204, s1, v198
	v_add_u32_e32 v205, s1, v199
	s_barrier
	s_cmpk_eq_i32 s10, 0x700
	s_cselect_b64 s[18:19], -1, 0
	s_cmpk_lg_i32 s10, 0x700
	s_cselect_b64 s[24:25], -1, 0
	s_add_u32 s49, s16, s10
	s_addc_u32 s50, s9, s11
	s_add_u32 s46, s8, s10
	s_addc_u32 s47, s3, s11
	s_add_u32 s20, s46, 0x100
	s_addc_u32 s48, s47, 0
	s_add_u32 s12, s49, 0x40080
	s_addc_u32 s0, s50, 0
	s_and_b32 s13, s0, 0xffff
	v_add_u32_e32 v207, 0x1c000, v198
	v_add_u32_e32 v208, 0x1c000, v199
	v_add_u32_e32 v209, 0x18000, v198
	v_add_u32_e32 v210, 0x18000, v199
	s_branch .LBB4_14

.LBB4_16:
	s_barrier
	s_waitcnt lgkmcnt(0)
	s_setprio 1
	v_mfma_f32_16x16x128_f8f6f4 v[180:183], v[24:31], v[56:63], v[180:183]
	s_add_u32 s12, s49, 0x100
	s_addc_u32 s21, s50, 0
	v_mfma_f32_16x16x128_f8f6f4 v[176:179], v[16:23], v[56:63], v[176:179]
	v_mfma_f32_16x16x128_f8f6f4 v[164:167], v[24:31], v[48:55], v[164:167]
	v_mfma_f32_16x16x128_f8f6f4 v[160:163], v[16:23], v[48:55], v[160:163]
	v_mfma_f32_16x16x128_f8f6f4 v[148:151], v[24:31], v[40:47], v[148:151]
	v_mfma_f32_16x16x128_f8f6f4 v[144:147], v[16:23], v[40:47], v[144:147]
	v_mfma_f32_16x16x128_f8f6f4 v[132:135], v[24:31], v[32:39], v[132:135]
	v_mfma_f32_16x16x128_f8f6f4 v[128:131], v[16:23], v[32:39], v[128:131]
	s_setprio 0
	s_barrier
	ds_read_b128 v[56:59], v200 offset:16384
	ds_read_b128 v[48:51], v200 offset:18432
	ds_read_b128 v[60:63], v201 offset:16384
	ds_read_b128 v[52:55], v201 offset:18432
	ds_read_b128 v[40:43], v200 offset:20480
	ds_read_b128 v[32:35], v200 offset:22528
	ds_read_b128 v[44:47], v201 offset:20480
	ds_read_b128 v[36:39], v201 offset:22528
	s_not_b64 s[0:1], s[24:25]
	s_andn2_b64 vcc, exec, s[24:25]
	s_cbranch_vccnz .LBB4_18
	s_and_b32 s13, s21, 0xffff
	s_mov_b32 m0, s7
	s_nop 0
	buffer_load_dwordx4 v192, s[12:15], 0 offen lds
	s_mov_b32 m0, s30
	s_nop 0
	buffer_load_dwordx4 v194, s[12:15], 0 offen lds

.LBB4_22:
	s_barrier
	s_setprio 1
	v_mfma_f32_16x16x128_f8f6f4 v[116:119], v[24:31], v[56:63], v[116:119]
	v_mfma_f32_16x16x128_f8f6f4 v[112:115], v[16:23], v[56:63], v[112:115]
	v_mfma_f32_16x16x128_f8f6f4 v[100:103], v[24:31], v[48:55], v[100:103]
	v_mfma_f32_16x16x128_f8f6f4 v[96:99], v[16:23], v[48:55], v[96:99]
	v_mfma_f32_16x16x128_f8f6f4 v[84:87], v[24:31], v[40:47], v[84:87]
	v_mfma_f32_16x16x128_f8f6f4 v[80:83], v[16:23], v[40:47], v[80:83]
	v_mfma_f32_16x16x128_f8f6f4 v[68:71], v[24:31], v[32:39], v[68:71]
	v_mfma_f32_16x16x128_f8f6f4 v[64:67], v[16:23], v[32:39], v[64:67]
	s_setprio 0
	s_barrier
	ds_read_b128 v[8:11], v209
	ds_read_b128 v[0:3], v209 offset:2048
	ds_read_b128 v[12:15], v210
	ds_read_b128 v[4:7], v210 offset:2048
	ds_read_b128 v[56:59], v200 offset:32768
	ds_read_b128 v[48:51], v200 offset:34816
	ds_read_b128 v[60:63], v201 offset:32768
	ds_read_b128 v[52:55], v201 offset:34816
	ds_read_b128 v[40:43], v200 offset:36864
	ds_read_b128 v[32:35], v200 offset:38912
	ds_read_b128 v[44:47], v201 offset:36864
	ds_read_b128 v[36:39], v201 offset:38912
	s_waitcnt vmcnt(8)
	s_and_b64 vcc, exec, s[0:1]
	s_cbranch_vccnz .LBB4_24
	s_add_u32 s52, s49, 0x40100
	s_addc_u32 s13, s50, 0
	s_and_b32 s53, s13, 0xffff
	s_mov_b32 s54, s14
	s_mov_b32 s55, s15
	s_mov_b32 m0, s34
	s_nop 0
	buffer_load_dwordx4 v192, s[52:55], 0 offen lds
	s_mov_b32 m0, s35
	s_nop 0
	buffer_load_dwordx4 v194, s[52:55], 0 offen lds

	.amdhsa_kernel _ZN2rb6k_gemmILi1ENS_6SchedGILb1EEENS_5EpiP3EEEvT0_T1_
		.amdhsa_group_segment_fixed_size 0
		.amdhsa_private_segment_fixed_size 0
		.amdhsa_kernarg_size 48
		.amdhsa_user_sgpr_count 2
		.amdhsa_user_sgpr_dispatch_ptr 0
		.amdhsa_user_sgpr_queue_ptr 0
		.amdhsa_user_sgpr_kernarg_segment_ptr 1
		.amdhsa_user_sgpr_dispatch_id 0
		.amdhsa_user_sgpr_kernarg_preload_length 0
		.amdhsa_user_sgpr_kernarg_preload_offset 0
		.amdhsa_user_sgpr_private_segment_size 0
		.amdhsa_uses_dynamic_stack 0
		.amdhsa_enable_private_segment 0
		.amdhsa_system_sgpr_workgroup_id_x 1
		.amdhsa_system_sgpr_workgroup_id_y 0
		.amdhsa_system_sgpr_workgroup_id_z 0
		.amdhsa_system_sgpr_workgroup_info 0
		.amdhsa_system_vgpr_workitem_id 0
		.amdhsa_next_free_vgpr 211
		.amdhsa_next_free_sgpr 56
		.amdhsa_accum_offset 212
		.amdhsa_reserve_vcc 1
		.amdhsa_float_round_mode_32 0
		.amdhsa_float_round_mode_16_64 0
		.amdhsa_float_denorm_mode_32 3
		.amdhsa_float_denorm_mode_16_64 3
		.amdhsa_dx10_clamp 1
		.amdhsa_ieee_mode 1
		.amdhsa_fp16_overflow 0
		.amdhsa_tg_split 0
		.amdhsa_exception_fp_ieee_invalid_op 0
		.amdhsa_exception_fp_denorm_src 0
		.amdhsa_exception_fp_ieee_div_zero 0
		.amdhsa_exception_fp_ieee_overflow 0
		.amdhsa_exception_fp_ieee_underflow 0
		.amdhsa_exception_fp_ieee_inexact 0
		.amdhsa_exception_int_div_zero 0
	.end_amdhsa_kernel

.LBB5_16:
	s_and_b32 s35, s20, 3
	s_add_u32 s8, s12, 0x80
	s_load_dword s2, s[0:1], 0x48
	s_addc_u32 s0, s7, 0
	s_add_i32 s37, s25, 0x18000
	s_and_b32 s9, s0, 0xffff
	s_mov_b32 m0, s37
	s_add_i32 s38, s25, 0x1a000
	s_waitcnt vmcnt(4)
	s_barrier
	buffer_load_dwordx4 v192, s[8:11], 0 offen lds
	s_mov_b32 m0, s38
	v_lshrrev_b32_e32 v1, 4, v0
	buffer_load_dwordx4 v193, s[8:11], 0 offen lds
	s_add_u32 s8, s16, 0x80
	s_addc_u32 s0, s13, 0
	s_add_i32 s39, s25, 0x8000
	s_and_b32 s9, s0, 0xffff
	s_mov_b32 m0, s39
	s_add_i32 s40, s25, 0xa000
	buffer_load_dwordx4 v192, s[8:11], 0 offen lds
	s_mov_b32 m0, s40
	v_and_b32_e32 v194, 15, v0
	buffer_load_dwordx4 v193, s[8:11], 0 offen lds
	s_add_u32 s8, s12, 0x40080
	s_addc_u32 s0, s7, 0
	s_add_i32 s41, s25, 0x1c000
	s_and_b32 s9, s0, 0xffff
	s_mov_b32 m0, s41
	s_add_i32 s42, s25, 0x1e000
	buffer_load_dwordx4 v192, s[8:11], 0 offen lds
	s_mov_b32 m0, s42
	v_bfe_u32 v195, v0, 4, 2
	buffer_load_dwordx4 v193, s[8:11], 0 offen lds
	v_bfe_u32 v0, v0, 1, 3
	v_bitop3_b32 v0, v1, v0, 3 bitop3:0x6c
	v_lshlrev_b32_e32 v1, 7, v194
	v_lshlrev_b32_e32 v0, 4, v0
	v_lshl_or_b32 v2, s3, 13, v1
	v_lshl_or_b32 v1, s35, 12, v1
	s_waitcnt vmcnt(6)
	v_or_b32_e32 v3, v2, v0
	v_or_b32_e32 v196, v1, v0
	v_bitop3_b32 v2, v2, 64, v0 bitop3:0x36
	v_bitop3_b32 v197, v1, 64, v0 bitop3:0x36
	v_mov_b32_e32 v64, 0
	s_add_i32 s0, 0, 0x10000
	s_add_i32 s1, 0, 0x14000
	s_add_i32 s43, s25, 0xc000
	s_add_i32 s44, s25, 0xe000
	s_mov_b32 s45, -2
	s_mov_b64 s[14:15], 0
	v_add_u32_e32 v198, 0, v3
	v_add_u32_e32 v199, 0, v2
	s_add_i32 s46, 0, 0x18000
	v_mov_b32_e32 v65, v64
	v_mov_b32_e32 v66, v64
	v_mov_b32_e32 v67, v64
	v_mov_b32_e32 v68, v64
	v_mov_b32_e32 v69, v64
	v_mov_b32_e32 v70, v64
	v_mov_b32_e32 v71, v64
	v_mov_b32_e32 v76, v64
	v_mov_b32_e32 v77, v64
	v_mov_b32_e32 v78, v64
	v_mov_b32_e32 v79, v64
	v_mov_b32_e32 v80, v64
	v_mov_b32_e32 v81, v64
	v_mov_b32_e32 v82, v64
	v_mov_b32_e32 v83, v64
	v_mov_b32_e32 v88, v64
	v_mov_b32_e32 v89, v64
	v_mov_b32_e32 v90, v64
	v_mov_b32_e32 v91, v64
	v_mov_b32_e32 v92, v64
	v_mov_b32_e32 v93, v64
	v_mov_b32_e32 v94, v64
	v_mov_b32_e32 v95, v64
	v_mov_b32_e32 v104, v64
	v_mov_b32_e32 v105, v64
	v_mov_b32_e32 v106, v64
	v_mov_b32_e32 v107, v64
	v_mov_b32_e32 v108, v64
	v_mov_b32_e32 v109, v64
	v_mov_b32_e32 v110, v64
	v_mov_b32_e32 v111, v64
	v_mov_b32_e32 v72, v64
	v_mov_b32_e32 v73, v64
	v_mov_b32_e32 v74, v64
	v_mov_b32_e32 v75, v64
	v_mov_b32_e32 v84, v64
	v_mov_b32_e32 v85, v64
	v_mov_b32_e32 v86, v64
	v_mov_b32_e32 v87, v64
	v_mov_b32_e32 v96, v64
	v_mov_b32_e32 v97, v64
	v_mov_b32_e32 v98, v64
	v_mov_b32_e32 v99, v64
	v_mov_b32_e32 v100, v64
	v_mov_b32_e32 v101, v64
	v_mov_b32_e32 v102, v64
	v_mov_b32_e32 v103, v64
	v_mov_b32_e32 v112, v64
	v_mov_b32_e32 v113, v64
	v_mov_b32_e32 v114, v64
	v_mov_b32_e32 v115, v64
	v_mov_b32_e32 v116, v64
	v_mov_b32_e32 v117, v64
	v_mov_b32_e32 v118, v64
	v_mov_b32_e32 v119, v64
	v_mov_b32_e32 v120, v64
	v_mov_b32_e32 v121, v64
	v_mov_b32_e32 v122, v64
	v_mov_b32_e32 v123, v64
	v_mov_b32_e32 v124, v64
	v_mov_b32_e32 v125, v64
	v_mov_b32_e32 v126, v64
	v_mov_b32_e32 v127, v64
	v_mov_b32_e32 v128, v64
	v_mov_b32_e32 v129, v64
	v_mov_b32_e32 v130, v64
	v_mov_b32_e32 v131, v64
	v_mov_b32_e32 v132, v64
	v_mov_b32_e32 v133, v64
	v_mov_b32_e32 v134, v64
	v_mov_b32_e32 v135, v64
	v_mov_b32_e32 v140, v64
	v_mov_b32_e32 v141, v64
	v_mov_b32_e32 v142, v64
	v_mov_b32_e32 v143, v64
	v_mov_b32_e32 v148, v64
	v_mov_b32_e32 v149, v64
	v_mov_b32_e32 v150, v64
	v_mov_b32_e32 v151, v64
	v_mov_b32_e32 v156, v64
	v_mov_b32_e32 v157, v64
	v_mov_b32_e32 v158, v64
	v_mov_b32_e32 v159, v64
	v_mov_b32_e32 v164, v64
	v_mov_b32_e32 v165, v64
	v_mov_b32_e32 v166, v64
	v_mov_b32_e32 v167, v64
	v_mov_b32_e32 v172, v64
	v_mov_b32_e32 v173, v64
	v_mov_b32_e32 v174, v64
	v_mov_b32_e32 v175, v64
	v_mov_b32_e32 v180, v64
	v_mov_b32_e32 v181, v64
	v_mov_b32_e32 v182, v64
	v_mov_b32_e32 v183, v64
	v_mov_b32_e32 v136, v64
	v_mov_b32_e32 v137, v64
	v_mov_b32_e32 v138, v64
	v_mov_b32_e32 v139, v64
	v_mov_b32_e32 v144, v64
	v_mov_b32_e32 v145, v64
	v_mov_b32_e32 v146, v64
	v_mov_b32_e32 v147, v64
	v_mov_b32_e32 v152, v64
	v_mov_b32_e32 v153, v64
	v_mov_b32_e32 v154, v64
	v_mov_b32_e32 v155, v64
	v_mov_b32_e32 v160, v64
	v_mov_b32_e32 v161, v64
	v_mov_b32_e32 v162, v64
	v_mov_b32_e32 v163, v64
	v_mov_b32_e32 v168, v64
	v_mov_b32_e32 v169, v64
	v_mov_b32_e32 v170, v64
	v_mov_b32_e32 v171, v64
	v_mov_b32_e32 v176, v64
	v_mov_b32_e32 v177, v64
	v_mov_b32_e32 v178, v64
	v_mov_b32_e32 v179, v64
	v_mov_b32_e32 v184, v64
	v_mov_b32_e32 v185, v64
	v_mov_b32_e32 v186, v64
	v_mov_b32_e32 v187, v64
	v_mov_b32_e32 v188, v64
	v_mov_b32_e32 v189, v64
	v_mov_b32_e32 v190, v64
	v_mov_b32_e32 v191, v64
	v_add_u32_e32 v200, s0, v196
	v_add_u32_e32 v201, s0, v197
	v_add_u32_e32 v202, s1, v196
	v_add_u32_e32 v203, s1, v197
	s_barrier
	s_cmpk_eq_i32 s14, 0x700
	s_cselect_b64 s[18:19], -1, 0
	s_cmpk_lg_i32 s14, 0x700
	s_cselect_b64 s[26:27], -1, 0
	s_add_u32 s50, s16, s14
	s_addc_u32 s51, s13, s15
	s_add_u32 s47, s12, s14
	s_addc_u32 s48, s7, s15
	s_add_u32 s20, s47, 0x100
	s_addc_u32 s49, s48, 0
	s_add_u32 s8, s50, 0x40080
	s_addc_u32 s0, s51, 0
	s_and_b32 s9, s0, 0xffff
	v_add_u32_e32 v205, 0x1c000, v196
	v_add_u32_e32 v206, 0x1c000, v197
	v_add_u32_e32 v207, 0x18000, v196
	v_add_u32_e32 v208, 0x18000, v197
	s_branch .LBB5_18

.LBB5_20:
	s_barrier
	s_waitcnt lgkmcnt(0)
	s_setprio 1
	v_mfma_f32_16x16x128_f8f6f4 v[180:183], v[24:31], v[56:63], v[180:183]
	s_add_u32 s8, s50, 0x100
	s_addc_u32 s21, s51, 0
	v_mfma_f32_16x16x128_f8f6f4 v[172:175], v[16:23], v[56:63], v[172:175]
	v_mfma_f32_16x16x128_f8f6f4 v[164:167], v[24:31], v[48:55], v[164:167]
	v_mfma_f32_16x16x128_f8f6f4 v[156:159], v[16:23], v[48:55], v[156:159]
	v_mfma_f32_16x16x128_f8f6f4 v[148:151], v[24:31], v[40:47], v[148:151]
	v_mfma_f32_16x16x128_f8f6f4 v[140:143], v[16:23], v[40:47], v[140:143]
	v_mfma_f32_16x16x128_f8f6f4 v[132:135], v[24:31], v[32:39], v[132:135]
	v_mfma_f32_16x16x128_f8f6f4 v[128:131], v[16:23], v[32:39], v[128:131]
	s_setprio 0
	s_barrier
	ds_read_b128 v[56:59], v198 offset:16384
	ds_read_b128 v[48:51], v198 offset:18432
	ds_read_b128 v[60:63], v199 offset:16384
	ds_read_b128 v[52:55], v199 offset:18432
	ds_read_b128 v[40:43], v198 offset:20480
	ds_read_b128 v[32:35], v198 offset:22528
	ds_read_b128 v[44:47], v199 offset:20480
	ds_read_b128 v[36:39], v199 offset:22528
	s_not_b64 s[0:1], s[26:27]
	s_andn2_b64 vcc, exec, s[26:27]
	s_cbranch_vccnz .LBB5_22
	s_and_b32 s9, s21, 0xffff
	s_mov_b32 m0, s25
	s_nop 0
	buffer_load_dwordx4 v192, s[8:11], 0 offen lds
	s_mov_b32 m0, s31
	s_nop 0
	buffer_load_dwordx4 v193, s[8:11], 0 offen lds

.LBB5_26:
	s_barrier
	s_setprio 1
	v_mfma_f32_16x16x128_f8f6f4 v[108:111], v[24:31], v[56:63], v[108:111]
	v_mfma_f32_16x16x128_f8f6f4 v[104:107], v[16:23], v[56:63], v[104:107]
	v_mfma_f32_16x16x128_f8f6f4 v[92:95], v[24:31], v[48:55], v[92:95]
	v_mfma_f32_16x16x128_f8f6f4 v[88:91], v[16:23], v[48:55], v[88:91]
	v_mfma_f32_16x16x128_f8f6f4 v[80:83], v[24:31], v[40:47], v[80:83]
	v_mfma_f32_16x16x128_f8f6f4 v[76:79], v[16:23], v[40:47], v[76:79]
	v_mfma_f32_16x16x128_f8f6f4 v[68:71], v[24:31], v[32:39], v[68:71]
	v_mfma_f32_16x16x128_f8f6f4 v[64:67], v[16:23], v[32:39], v[64:67]
	s_setprio 0
	s_barrier
	ds_read_b128 v[8:11], v207
	ds_read_b128 v[0:3], v207 offset:2048
	ds_read_b128 v[12:15], v208
	ds_read_b128 v[4:7], v208 offset:2048
	ds_read_b128 v[56:59], v198 offset:32768
	ds_read_b128 v[48:51], v198 offset:34816
	ds_read_b128 v[60:63], v199 offset:32768
	ds_read_b128 v[52:55], v199 offset:34816
	ds_read_b128 v[40:43], v198 offset:36864
	ds_read_b128 v[32:35], v198 offset:38912
	ds_read_b128 v[44:47], v199 offset:36864
	ds_read_b128 v[36:39], v199 offset:38912
	s_waitcnt vmcnt(8)
	s_and_b64 vcc, exec, s[0:1]
	s_cbranch_vccnz .LBB5_28
	s_add_u32 s52, s50, 0x40100
	s_addc_u32 s9, s51, 0
	s_and_b32 s53, s9, 0xffff
	s_mov_b32 s54, s10
	s_mov_b32 s55, s11
	s_mov_b32 m0, s34
	s_nop 0
	buffer_load_dwordx4 v192, s[52:55], 0 offen lds
	s_mov_b32 m0, s36
	s_nop 0
	buffer_load_dwordx4 v193, s[52:55], 0 offen lds

	.amdhsa_kernel _ZN2rb6k_gemmILi1ENS_6SchedGILb1EEENS_6EpiOutEEEvT0_T1_
		.amdhsa_group_segment_fixed_size 0
		.amdhsa_private_segment_fixed_size 0
		.amdhsa_kernarg_size 80
		.amdhsa_user_sgpr_count 2
		.amdhsa_user_sgpr_dispatch_ptr 0
		.amdhsa_user_sgpr_queue_ptr 0
		.amdhsa_user_sgpr_kernarg_segment_ptr 1
		.amdhsa_user_sgpr_dispatch_id 0
		.amdhsa_user_sgpr_kernarg_preload_length 0
		.amdhsa_user_sgpr_kernarg_preload_offset 0
		.amdhsa_user_sgpr_private_segment_size 0
		.amdhsa_uses_dynamic_stack 0
		.amdhsa_enable_private_segment 0
		.amdhsa_system_sgpr_workgroup_id_x 1
		.amdhsa_system_sgpr_workgroup_id_y 0
		.amdhsa_system_sgpr_workgroup_id_z 0
		.amdhsa_system_sgpr_workgroup_info 0
		.amdhsa_system_vgpr_workitem_id 0
		.amdhsa_next_free_vgpr 209
		.amdhsa_next_free_sgpr 56
		.amdhsa_accum_offset 212
		.amdhsa_reserve_vcc 1
		.amdhsa_float_round_mode_32 0
		.amdhsa_float_round_mode_16_64 0
		.amdhsa_float_denorm_mode_32 3
		.amdhsa_float_denorm_mode_16_64 3
		.amdhsa_dx10_clamp 1
		.amdhsa_ieee_mode 1
		.amdhsa_fp16_overflow 0
		.amdhsa_tg_split 0
		.amdhsa_exception_fp_ieee_invalid_op 0
		.amdhsa_exception_fp_denorm_src 0
		.amdhsa_exception_fp_ieee_div_zero 0
		.amdhsa_exception_fp_ieee_overflow 0
		.amdhsa_exception_fp_ieee_underflow 0
		.amdhsa_exception_fp_ieee_inexact 0
		.amdhsa_exception_int_div_zero 0
	.end_amdhsa_kernel

.LBB6_18:
	s_add_u32 s8, s50, 0xfffc0080
	s_addc_u32 s9, s51, -1
	s_barrier
	s_waitcnt lgkmcnt(0)
	s_and_b64 s[0:1], s[0:1], exec
	s_cselect_b32 s13, s9, s46
	s_cselect_b32 s8, s8, s47
	s_setprio 1
	s_waitcnt lgkmcnt(3)
	v_mfma_i32_16x16x64_i8 v[92:95], v[128:131], v[184:187], v[92:95]
	s_waitcnt lgkmcnt(2)
	v_mfma_i32_16x16x64_i8 v[88:91], v[132:135], v[184:187], v[88:91]
	v_mfma_i32_16x16x64_i8 v[84:87], v[128:131], v[172:175], v[84:87]
	v_mfma_i32_16x16x64_i8 v[80:83], v[132:135], v[172:175], v[80:83]
	v_mfma_i32_16x16x64_i8 v[76:79], v[128:131], v[168:171], v[76:79]
	v_mfma_i32_16x16x64_i8 v[72:75], v[132:135], v[168:171], v[72:75]
	v_mfma_i32_16x16x64_i8 v[68:71], v[128:131], v[160:163], v[68:71]
	v_mfma_i32_16x16x64_i8 v[64:67], v[132:135], v[160:163], v[64:67]
	s_waitcnt lgkmcnt(1)
	v_mfma_i32_16x16x64_i8 v[92:95], v[140:143], v[188:191], v[92:95]
	s_waitcnt lgkmcnt(0)
	v_mfma_i32_16x16x64_i8 v[88:91], v[136:139], v[188:191], v[88:91]
	v_mfma_i32_16x16x64_i8 v[84:87], v[140:143], v[176:179], v[84:87]
	v_mfma_i32_16x16x64_i8 v[80:83], v[136:139], v[176:179], v[80:83]
	v_mfma_i32_16x16x64_i8 v[76:79], v[140:143], v[180:183], v[76:79]
	v_mfma_i32_16x16x64_i8 v[72:75], v[136:139], v[180:183], v[72:75]
	v_mfma_i32_16x16x64_i8 v[68:71], v[140:143], v[164:167], v[68:71]
	v_mfma_i32_16x16x64_i8 v[64:67], v[136:139], v[164:167], v[64:67]
	s_setprio 0
	s_barrier
	ds_read_b128 v[184:187], v200 offset:16384
	ds_read_b128 v[172:175], v200 offset:18432
	ds_read_b128 v[188:191], v201 offset:16384
	ds_read_b128 v[176:179], v201 offset:18432
	ds_read_b128 v[168:171], v200 offset:20480
	ds_read_b128 v[160:163], v200 offset:22528
	ds_read_b128 v[180:183], v201 offset:20480
	ds_read_b128 v[164:167], v201 offset:22528
	s_not_b64 s[0:1], s[22:23]
	s_andn2_b64 vcc, exec, s[22:23]
	s_cbranch_vccnz .LBB6_20
	s_and_b32 s9, s13, 0xffff
	s_mov_b32 m0, s25
	s_nop 0
	buffer_load_dwordx4 v192, s[8:11], 0 offen lds
	s_mov_b32 m0, s28
	s_nop 0
	buffer_load_dwordx4 v194, s[8:11], 0 offen lds

amdhsa.kernels:
  - .agpr_count:     0
    .args:
      - .actual_access:  read_only
        .address_space:  global
        .offset:         0
        .size:           8
        .value_kind:     global_buffer
      - .actual_access:  read_only
        .address_space:  global
        .offset:         8
        .size:           8
        .value_kind:     global_buffer
      - .actual_access:  read_only
        .address_space:  global
        .offset:         16
        .size:           8
        .value_kind:     global_buffer
      - .actual_access:  read_only
        .address_space:  global
        .offset:         24
        .size:           8
        .value_kind:     global_buffer
      - .actual_access:  read_only
        .address_space:  global
        .offset:         32
        .size:           8
        .value_kind:     global_buffer
      - .actual_access:  read_only
        .address_space:  global
        .offset:         40
        .size:           8
        .value_kind:     global_buffer
      - .actual_access:  read_only
        .address_space:  global
        .offset:         48
        .size:           8
        .value_kind:     global_buffer
      - .actual_access:  read_only
        .address_space:  global
        .offset:         56
        .size:           8
        .value_kind:     global_buffer
      - .actual_access:  write_only
        .address_space:  global
        .offset:         64
        .size:           8
        .value_kind:     global_buffer
      - .offset:         72
        .size:           4
        .value_kind:     by_value
    .group_segment_fixed_size: 32768
    .kernarg_segment_align: 8
    .kernarg_segment_size: 76
    .language:       OpenCL C
    .language_version:
      - 2
      - 0
    .max_flat_workgroup_size: 256
    .name:           _ZN2rb6k_prepEPKfS1_S1_S1_S1_S1_S1_S1_Phi
    .private_segment_fixed_size: 0
    .sgpr_count:     22
    .sgpr_spill_count: 0
    .symbol:         _ZN2rb6k_prepEPKfS1_S1_S1_S1_S1_S1_S1_Phi.kd
    .uniform_work_group_size: 1
    .uses_dynamic_stack: false
    .vgpr_count:     100
    .vgpr_spill_count: 0
    .wavefront_size: 64
  - .agpr_count:     0
    .args:
      - .address_space:  global
        .offset:         0
        .size:           8
        .value_kind:     global_buffer
      - .actual_access:  read_only
        .address_space:  global
        .offset:         8
        .size:           8
        .value_kind:     global_buffer
    .group_segment_fixed_size: 0
    .kernarg_segment_align: 8
    .kernarg_segment_size: 16
    .language:       OpenCL C
    .language_version:
      - 2
      - 0
    .max_flat_workgroup_size: 256
    .name:           _ZN2rb5k_midEPhPKf
    .private_segment_fixed_size: 0
    .sgpr_count:     20
    .sgpr_spill_count: 0
    .symbol:         _ZN2rb5k_midEPhPKf.kd
    .uniform_work_group_size: 1
    .uses_dynamic_stack: false
    .vgpr_count:     86
    .vgpr_spill_count: 0
    .wavefront_size: 64
  - .agpr_count:     0
    .args:
      - .offset:         0
        .size:           24
        .value_kind:     by_value
      - .offset:         24
        .size:           64
        .value_kind:     by_value
    .group_segment_fixed_size: 0
    .kernarg_segment_align: 8
    .kernarg_segment_size: 88
    .language:       OpenCL C
    .language_version:
      - 2
      - 0
    .max_flat_workgroup_size: 512
    .name:           _ZN2rb6k_gemmILi2ENS_7SchedP1ENS_5EpiP1EEEvT0_T1_
    .private_segment_fixed_size: 0
    .sgpr_count:     86
    .sgpr_spill_count: 0
    .symbol:         _ZN2rb6k_gemmILi2ENS_7SchedP1ENS_5EpiP1EEEvT0_T1_.kd
    .uniform_work_group_size: 1
    .uses_dynamic_stack: false
    .vgpr_count:     214
    .vgpr_spill_count: 0
    .wavefront_size: 64
  - .agpr_count:     0
    .args:
      - .offset:         0
        .size:           24
        .value_kind:     by_value
      - .offset:         24
        .size:           16
        .value_kind:     by_value
    .group_segment_fixed_size: 0
    .kernarg_segment_align: 8
    .kernarg_segment_size: 40
    .language:       OpenCL C
    .language_version:
      - 2
      - 0
    .max_flat_workgroup_size: 512
    .name:           _ZN2rb6k_gemmILi1ENS_7SchedP2ENS_7EpiSlabEEEvT0_T1_
    .private_segment_fixed_size: 0
    .sgpr_count:     73
    .sgpr_spill_count: 0
    .symbol:         _ZN2rb6k_gemmILi1ENS_7SchedP2ENS_7EpiSlabEEEvT0_T1_.kd
    .uniform_work_group_size: 1
    .uses_dynamic_stack: false
    .vgpr_count:     214
    .vgpr_spill_count: 0
    .wavefront_size: 64
  - .agpr_count:     0
    .args:
      - .offset:         0
        .size:           32
        .value_kind:     by_value
      - .offset:         32
        .size:           16
        .value_kind:     by_value
    .group_segment_fixed_size: 0
    .kernarg_segment_align: 8
    .kernarg_segment_size: 48
    .language:       OpenCL C
    .language_version:
      - 2
      - 0
    .max_flat_workgroup_size: 512
    .name:           _ZN2rb6k_gemmILi1ENS_6SchedGILb1EEENS_5EpiP3EEEvT0_T1_
    .private_segment_fixed_size: 0
    .sgpr_count:     62
    .sgpr_spill_count: 0
    .symbol:         _ZN2rb6k_gemmILi1ENS_6SchedGILb1EEENS_5EpiP3EEEvT0_T1_.kd
    .uniform_work_group_size: 1
    .uses_dynamic_stack: false
    .vgpr_count:     211
    .vgpr_spill_count: 0
    .wavefront_size: 64
  - .agpr_count:     0
    .args:
      - .offset:         0
        .size:           32
        .value_kind:     by_value
      - .offset:         32
        .size:           48
        .value_kind:     by_value
    .group_segment_fixed_size: 0
    .kernarg_segment_align: 8
    .kernarg_segment_size: 80
    .language:       OpenCL C
    .language_version:
      - 2
      - 0
    .max_flat_workgroup_size: 512
    .name:           _ZN2rb6k_gemmILi1ENS_6SchedGILb1EEENS_6EpiOutEEEvT0_T1_
    .private_segment_fixed_size: 0
    .sgpr_count:     62
    .sgpr_spill_count: 0
    .symbol:         _ZN2rb6k_gemmILi1ENS_6SchedGILb1EEENS_6EpiOutEEEvT0_T1_.kd
    .uniform_work_group_size: 1
    .uses_dynamic_stack: false
    .vgpr_count:     209
    .vgpr_spill_count: 0
    .wavefront_size: 64
  - .agpr_count:     0
    .args:
      - .offset:         0
        .size:           24
        .value_kind:     by_value
      - .offset:         24
        .size:           1
        .value_kind:     by_value
    .group_segment_fixed_size: 0
    .kernarg_segment_align: 8
    .kernarg_segment_size: 28
    .language:       OpenCL C
    .language_version:
      - 2
      - 0
    .max_flat_workgroup_size: 512
    .name:           _ZN2rb6k_gemmILi2ENS_7SchedP1ENS_7EpiNullEEEvT0_T1_
    .private_segment_fixed_size: 0
    .sgpr_count:     66
    .sgpr_spill_count: 0
    .symbol:         _ZN2rb6k_gemmILi2ENS_7SchedP1ENS_7EpiNullEEEvT0_T1_.kd
    .uniform_work_group_size: 1
    .uses_dynamic_stack: false
    .vgpr_count:     205
    .vgpr_spill_count: 0
    .wavefront_size: 64
